# prep row loop: loads two batches ahead (second prefetch buffer in unused VGPRs), counted vmcnt instead of vmcnt(0) behind the stores, first prefetch issued with the first batch
# baseline (speedup 1.0000x reference)
.LBB0_453:
	s_movk_i32 s13, 0x3000
	v_add_co_u32_e32 v10, vcc, s13, v4
	s_movk_i32 s13, 0x6000
	s_nop 0
	v_addc_co_u32_e32 v11, vcc, 0, v5, vcc
	v_add_co_u32_e32 v12, vcc, s13, v4
	s_mov_b32 s13, 0x9000
	s_nop 0
	v_addc_co_u32_e32 v13, vcc, 0, v5, vcc
	v_add_co_u32_e32 v14, vcc, s13, v4
	s_mov_b32 s13, 0xd000
	s_nop 0
	v_addc_co_u32_e32 v15, vcc, 0, v5, vcc
	global_load_dwordx4 v[6:9], v[4:5], off nt
	global_load_dwordx4 v[58:61], v[12:13], off offset:2048 nt
	global_load_dwordx4 v[54:57], v[14:15], off offset:3072 nt
	v_add_co_u32_e32 v12, vcc, s13, v4
	s_mov_b32 s13, 0x10000
	s_nop 0
	v_addc_co_u32_e32 v13, vcc, 0, v5, vcc
	v_add_co_u32_e32 v14, vcc, s13, v4
	s_mov_b32 s13, 0x16000
	s_nop 0
	v_addc_co_u32_e32 v15, vcc, 0, v5, vcc
	global_load_dwordx4 v[50:53], v[12:13], off nt
	global_load_dwordx4 v[46:49], v[14:15], off offset:1024 nt
	v_add_co_u32_e32 v12, vcc, s13, v4
	s_mov_b32 s13, 0x1a000
	s_nop 0
	v_addc_co_u32_e32 v13, vcc, 0, v5, vcc
	global_load_dwordx4 v[38:41], v[12:13], off offset:3072 nt
	v_add_co_u32_e32 v12, vcc, s13, v4
	s_mov_b32 s13, 0x13000
	s_nop 0
	v_addc_co_u32_e32 v13, vcc, 0, v5, vcc
	v_add_co_u32_e32 v4, vcc, s13, v4
	global_load_dwordx4 v[34:37], v[12:13], off nt
	s_nop 0
	v_addc_co_u32_e32 v5, vcc, 0, v5, vcc
	global_load_dwordx4 v[42:45], v[4:5], off offset:2048 nt
	global_load_dwordx4 v[62:65], v[10:11], off offset:1024 nt
	s_mov_b64 s[24:25], 0xa400
	v_lshl_add_u64 v[138:139], v[4:5], 0, s[24:25]
	global_load_dwordx4 v[138:141], v[138:139], off nt
	s_mov_b64 s[24:25], 0xd800
	v_lshl_add_u64 v[134:135], v[4:5], 0, s[24:25]
	global_load_dwordx4 v[134:137], v[134:135], off nt
	s_mov_b64 s[24:25], 0x10c00
	v_lshl_add_u64 v[142:143], v[4:5], 0, s[24:25]
	global_load_dwordx4 v[142:145], v[142:143], off nt
	s_mov_b64 s[24:25], 0x14000
	v_lshl_add_u64 v[146:147], v[4:5], 0, s[24:25]
	global_load_dwordx4 v[146:149], v[146:147], off nt
	s_mov_b64 s[24:25], 0x17400
	v_lshl_add_u64 v[150:151], v[4:5], 0, s[24:25]
	global_load_dwordx4 v[150:153], v[150:151], off nt
	s_mov_b64 s[24:25], 0x1a800
	v_lshl_add_u64 v[162:163], v[4:5], 0, s[24:25]
	global_load_dwordx4 v[162:165], v[162:163], off nt
	s_mov_b64 s[24:25], 0x1dc00
	v_lshl_add_u64 v[154:155], v[4:5], 0, s[24:25]
	global_load_dwordx4 v[154:157], v[154:155], off nt
	s_mov_b64 s[24:25], 0x21000
	v_lshl_add_u64 v[158:159], v[4:5], 0, s[24:25]
	global_load_dwordx4 v[158:161], v[158:159], off nt
	v_mov_b32_e32 v0, 0x300
	s_cmp_gt_i32 s11, 5
	v_lshl_add_u64 v[80:81], v[2:3], 1, s[6:7]
	v_mad_i64_i32 v[82:83], s[6:7], s4, v0, v[66:67]
	s_cselect_b64 s[56:57], -1, 0
	s_ashr_i32 s7, s11, 1
	s_and_b32 s11, s12, 0x200
	s_lshl_b32 s12, s7, 10
	s_ashr_i32 s13, s12, 31
	v_or_b32_e32 v0, s11, v100
	s_cmp_eq_u32 s7, 1
	v_lshlrev_b32_e32 v0, 1, v0
	s_cselect_b64 s[58:59], -1, 0
	s_lshl_b64 s[4:5], s[4:5], 13
	s_lshl_b64 s[12:13], s[12:13], 1
	v_or_b32_e32 v84, s4, v0
	s_add_u32 s4, s4, s12
	v_mov_b32_e32 v85, s5
	s_addc_u32 s5, s5, s13
	v_or_b32_e32 v86, s4, v0
	s_mov_b32 s6, 7
	v_mov_b32_e32 v87, s5
	s_waitcnt vmcnt(8)
	v_lshlrev_b32_e32 v115, 16, v6
	v_and_b32_e32 v114, 0xffff0000, v6
	v_lshlrev_b32_e32 v113, 16, v7
	v_and_b32_e32 v0, 0xffff0000, v7
	v_and_b32_e32 v95, 0xffff0000, v8
	v_lshlrev_b32_e32 v94, 16, v8
	v_and_b32_e32 v93, 0xffff0000, v9
	v_lshlrev_b32_e32 v92, 16, v9
	s_branch .LBB0_455
.LBB0_454:
	s_mov_b64 s[4:5], 0x1a000
	v_lshl_add_u64 v[80:81], v[80:81], 0, s[4:5]
	s_add_i32 s6, s6, 8
	s_mov_b64 s[4:5], 0x1800
	s_and_b64 vcc, exec, s[58:59]
	s_cbranch_vccnz .Lprep_w24
	s_waitcnt vmcnt(16)
	s_branch .Lprep_wd
.Lprep_w24:
	s_waitcnt vmcnt(24)
.Lprep_wd:
	s_bitcmp1_b32 s7, 3
	s_cbranch_scc1 .Lprep_cp_b1
	v_mov_b64_e32 v[36:37], v[160:161]
	v_mov_b64_e32 v[40:41], v[156:157]
	v_mov_b64_e32 v[44:45], v[164:165]
	v_mov_b64_e32 v[48:49], v[152:153]
	v_mov_b64_e32 v[52:53], v[148:149]
	v_mov_b64_e32 v[56:57], v[144:145]
	v_mov_b64_e32 v[60:61], v[136:137]
	v_mov_b64_e32 v[64:65], v[140:141]
	v_mov_b64_e32 v[34:35], v[158:159]
	v_mov_b64_e32 v[38:39], v[154:155]
	v_mov_b64_e32 v[42:43], v[162:163]
	v_mov_b64_e32 v[46:47], v[150:151]
	v_mov_b64_e32 v[50:51], v[146:147]
	v_mov_b64_e32 v[54:55], v[142:143]
	v_mov_b64_e32 v[58:59], v[134:135]
	v_mov_b64_e32 v[62:63], v[138:139]
	s_branch .Lprep_cpd
.Lprep_cp_b1:
	v_mov_b64_e32 v[36:37], v[28:29]
	v_mov_b64_e32 v[40:41], v[24:25]
	v_mov_b64_e32 v[44:45], v[32:33]
	v_mov_b64_e32 v[48:49], v[20:21]
	v_mov_b64_e32 v[52:53], v[16:17]
	v_mov_b64_e32 v[56:57], v[12:13]
	v_mov_b64_e32 v[60:61], v[4:5]
	v_mov_b64_e32 v[64:65], v[8:9]
	v_mov_b64_e32 v[34:35], v[26:27]
	v_mov_b64_e32 v[38:39], v[22:23]
	v_mov_b64_e32 v[42:43], v[30:31]
	v_mov_b64_e32 v[46:47], v[18:19]
	v_mov_b64_e32 v[50:51], v[14:15]
	v_mov_b64_e32 v[54:55], v[10:11]
	v_mov_b64_e32 v[58:59], v[2:3]
	v_mov_b64_e32 v[62:63], v[6:7]
.Lprep_cpd:
	v_lshl_add_u64 v[84:85], v[84:85], 0, s[60:61]
	v_lshl_add_u64 v[86:87], v[86:87], 0, s[60:61]
	v_lshl_add_u64 v[82:83], v[82:83], 0, s[4:5]
	s_cmp_lt_u32 s7, 56
	s_cbranch_scc0 .LBB0_430
.LBB0_455:
	s_add_i32 s7, s6, -7
	s_cmp_gt_u32 s7, 40
	s_cbranch_scc1 .LBB0_457
	s_bitcmp1_b32 s7, 3
	s_cbranch_scc1 .Lprep_ld_b2
	v_lshl_add_u64 v[22:23], s[50:51], 0, v[80:81]
	v_add_co_u32_e32 v2, vcc, 0x21238000, v22
	s_nop 1
	v_addc_co_u32_e32 v3, vcc, 0, v23, vcc
	v_add_co_u32_e32 v4, vcc, 0x2123c000, v22
	s_nop 1
	v_addc_co_u32_e32 v5, vcc, 0, v23, vcc
	v_add_co_u32_e32 v10, vcc, 0x2123f000, v22
	global_load_dwordx4 v[6:9], v[2:3], off offset:3072 nt
	s_nop 0
	global_load_dwordx4 v[2:5], v[4:5], off nt
	v_addc_co_u32_e32 v11, vcc, 0, v23, vcc
	v_add_co_u32_e32 v14, vcc, 0x21242000, v22
	s_nop 1
	v_addc_co_u32_e32 v15, vcc, 0, v23, vcc
	v_add_co_u32_e32 v18, vcc, 0x21245000, v22
	global_load_dwordx4 v[10:13], v[10:11], off offset:1024 nt
	s_nop 0
	global_load_dwordx4 v[14:17], v[14:15], off offset:2048 nt
	v_addc_co_u32_e32 v19, vcc, 0, v23, vcc
	v_add_co_u32_e32 v24, vcc, 0x21249000, v22
	s_nop 1
	v_addc_co_u32_e32 v25, vcc, 0, v23, vcc
	global_load_dwordx4 v[18:21], v[18:19], off offset:3072 nt
	s_nop 0
	global_load_dwordx4 v[30:33], v[24:25], off nt
	v_add_co_u32_e32 v24, vcc, 0x2124c000, v22
	s_nop 1
	v_addc_co_u32_e32 v25, vcc, 0, v23, vcc
	v_add_co_u32_e32 v26, vcc, 0x2124f000, v22
	s_nop 1
	v_addc_co_u32_e32 v27, vcc, 0, v23, vcc
	global_load_dwordx4 v[22:25], v[24:25], off offset:1024 nt
	s_nop 0
	global_load_dwordx4 v[26:29], v[26:27], off offset:2048 nt
	s_branch .LBB0_457
.Lprep_ld_b2:
	v_lshl_add_u64 v[154:155], s[50:51], 0, v[80:81]
	v_add_co_u32_e32 v134, vcc, 0x21238000, v154
	s_nop 1
	v_addc_co_u32_e32 v135, vcc, 0, v155, vcc
	v_add_co_u32_e32 v136, vcc, 0x2123c000, v154
	s_nop 1
	v_addc_co_u32_e32 v137, vcc, 0, v155, vcc
	v_add_co_u32_e32 v142, vcc, 0x2123f000, v154
	global_load_dwordx4 v[138:141], v[134:135], off offset:3072 nt
	s_nop 0
	global_load_dwordx4 v[134:137], v[136:137], off nt
	v_addc_co_u32_e32 v143, vcc, 0, v155, vcc
	v_add_co_u32_e32 v146, vcc, 0x21242000, v154
	s_nop 1
	v_addc_co_u32_e32 v147, vcc, 0, v155, vcc
	v_add_co_u32_e32 v150, vcc, 0x21245000, v154
	global_load_dwordx4 v[142:145], v[142:143], off offset:1024 nt
	s_nop 0
	global_load_dwordx4 v[146:149], v[146:147], off offset:2048 nt
	v_addc_co_u32_e32 v151, vcc, 0, v155, vcc
	v_add_co_u32_e32 v156, vcc, 0x21249000, v154
	s_nop 1
	v_addc_co_u32_e32 v157, vcc, 0, v155, vcc
	global_load_dwordx4 v[150:153], v[150:151], off offset:3072 nt
	s_nop 0
	global_load_dwordx4 v[162:165], v[156:157], off nt
	v_add_co_u32_e32 v156, vcc, 0x2124c000, v154
	s_nop 1
	v_addc_co_u32_e32 v157, vcc, 0, v155, vcc
	v_add_co_u32_e32 v158, vcc, 0x2124f000, v154
	s_nop 1
	v_addc_co_u32_e32 v159, vcc, 0, v155, vcc
	global_load_dwordx4 v[154:157], v[156:157], off offset:1024 nt
	s_nop 0
	global_load_dwordx4 v[158:161], v[158:159], off offset:2048 nt
